# stream tail trimmed (rows 0-6 selected and store address formed before the last row arrives) on top of v35
# baseline (speedup 1.0000x reference)
.LBB1_2:
	s_or_b64 exec, exec, s[0:1]
	s_lshr_b32 s8, s3, 6
	s_add_i32 s8, s8, s2
	s_and_b32 s8, s8, 15
	s_lshl_b32 s0, s2, 7
	v_and_b32_e32 v24, 63, v0
	s_add_i32 s9, s8, s0
	s_waitcnt lgkmcnt(0)
	s_and_b32 s1, s5, 0xffff
	s_mov_b32 s3, 0x20000
	s_brev_b32 s2, 16
	s_mov_b32 s0, s4
	v_lshlrev_b32_e32 v25, 4, v24
	s_lshl_b32 s4, s9, 12
	buffer_load_dwordx4 v[26:29], v25, s[0:3], s4 offen offset:1024 nt
	buffer_load_dwordx4 v[30:33], v25, s[0:3], s4 offen nt
	buffer_load_dwordx4 v[34:37], v25, s[0:3], s4 offen offset:2048 nt
	s_barrier
	s_add_i32 s5, s4, 0x10000
	buffer_load_dwordx4 v[38:41], v25, s[0:3], s5 offen offset:1024 nt
	buffer_load_dwordx4 v[42:45], v25, s[0:3], s5 offen nt
	buffer_load_dwordx4 v[16:19], v25, s[0:3], s4 offen offset:3072 nt
	s_add_i32 s10, s4, 0x20000
	buffer_load_dwordx4 v[46:49], v25, s[0:3], s5 offen offset:2048 nt
	buffer_load_dwordx4 v[20:23], v25, s[0:3], s5 offen offset:3072 nt
	buffer_load_dwordx4 v[50:53], v25, s[0:3], s10 offen offset:1024 nt
	buffer_load_dwordx4 v[54:57], v25, s[0:3], s10 offen nt
	ds_read_b128 v[4:7], v25 offset:1024
	ds_read_b128 v[0:3], v25
	ds_read_b128 v[12:15], v25 offset:2048
	ds_read_b128 v[8:11], v25 offset:3072
	s_add_i32 s5, s4, 0x30000
	v_cmp_gt_u32_e32 vcc, 8, v24
	s_waitcnt vmcnt(9) lgkmcnt(3)
	v_pk_mul_f32 v[28:29], v[6:7], v[28:29]
	v_pk_mul_f32 v[26:27], v[4:5], v[26:27]
	s_waitcnt vmcnt(8) lgkmcnt(2)
	v_pk_fma_f32 v[32:33], v[2:3], v[32:33], v[28:29]
	v_pk_fma_f32 v[30:31], v[0:1], v[30:31], v[26:27]
	buffer_load_dwordx4 v[26:29], v25, s[0:3], s5 offen offset:1024 nt
	s_waitcnt vmcnt(8) lgkmcnt(1)
	v_pk_fma_f32 v[58:59], v[14:15], v[36:37], v[32:33]
	v_pk_fma_f32 v[60:61], v[12:13], v[34:35], v[30:31]
	buffer_load_dwordx4 v[30:33], v25, s[0:3], s5 offen nt
	s_waitcnt vmcnt(8)
	v_pk_mul_f32 v[34:35], v[6:7], v[40:41]
	v_pk_mul_f32 v[36:37], v[4:5], v[38:39]
	s_waitcnt vmcnt(7)
	v_pk_fma_f32 v[44:45], v[2:3], v[44:45], v[34:35]
	v_pk_fma_f32 v[42:43], v[0:1], v[42:43], v[36:37]
	buffer_load_dwordx4 v[34:37], v25, s[0:3], s10 offen offset:2048 nt
	s_waitcnt vmcnt(4)
	v_pk_mul_f32 v[38:39], v[6:7], v[52:53]
	v_pk_mul_f32 v[40:41], v[4:5], v[50:51]
	s_waitcnt vmcnt(3)
	v_pk_fma_f32 v[50:51], v[2:3], v[56:57], v[38:39]
	v_pk_fma_f32 v[52:53], v[0:1], v[54:55], v[40:41]
	buffer_load_dwordx4 v[38:41], v25, s[0:3], s10 offen offset:3072 nt
	v_pk_fma_f32 v[48:49], v[14:15], v[48:49], v[44:45]
	v_pk_fma_f32 v[46:47], v[12:13], v[46:47], v[42:43]
	s_waitcnt lgkmcnt(0)
	v_pk_fma_f32 v[18:19], v[10:11], v[18:19], v[58:59]
	v_pk_fma_f32 v[16:17], v[8:9], v[16:17], v[60:61]
	v_add_f32_e32 v61, v18, v19
	v_add_f32_e32 v60, v16, v17
	v_pk_fma_f32 v[16:17], v[10:11], v[22:23], v[48:49]
	v_pk_fma_f32 v[18:19], v[8:9], v[20:21], v[46:47]
	v_add_f32_e32 v16, v16, v17
	v_add_f32_e32 v18, v18, v19
	v_add_f32_e32 v60, v60, v61
	v_add_f32_e32 v16, v18, v16
	s_add_i32 s10, s4, 0x50000
	s_waitcnt vmcnt(3)
	v_pk_mul_f32 v[28:29], v[6:7], v[28:29]
	v_pk_mul_f32 v[26:27], v[4:5], v[26:27]
	v_add_f32_dpp v16, v16, v16 quad_perm:[1,0,3,2] row_mask:0xf bank_mask:0xf bound_ctrl:1
	s_waitcnt vmcnt(2)
	v_pk_fma_f32 v[54:55], v[2:3], v[32:33], v[28:29]
	v_pk_fma_f32 v[56:57], v[0:1], v[30:31], v[26:27]
	buffer_load_dwordx4 v[26:29], v25, s[0:3], s5 offen offset:2048 nt
	buffer_load_dwordx4 v[30:33], v25, s[0:3], s5 offen offset:3072 nt
	s_add_i32 s5, s4, 0x40000
	buffer_load_dwordx4 v[42:45], v25, s[0:3], s5 offen offset:1024 nt
	s_waitcnt vmcnt(4)
	v_pk_fma_f32 v[50:51], v[14:15], v[36:37], v[50:51]
	v_pk_fma_f32 v[52:53], v[12:13], v[34:35], v[52:53]
	buffer_load_dwordx4 v[34:37], v25, s[0:3], s5 offen nt
	v_add_f32_dpp v16, v16, v16 quad_perm:[2,3,0,1] row_mask:0xf bank_mask:0xf bound_ctrl:1
	s_waitcnt vmcnt(4)
	v_pk_fma_f32 v[58:59], v[10:11], v[40:41], v[50:51]
	v_pk_fma_f32 v[38:39], v[8:9], v[38:39], v[52:53]
	v_add_f32_e32 v19, v58, v59
	v_add_f32_e32 v17, v38, v39
	v_add_f32_dpp v58, v60, v60 quad_perm:[1,0,3,2] row_mask:0xf bank_mask:0xf bound_ctrl:1
	v_add_f32_e32 v18, v17, v19
	v_add_f32_dpp v16, v16, v16 row_ror:4 row_mask:0xf bank_mask:0xf bound_ctrl:1
	v_add_f32_dpp v17, v58, v58 quad_perm:[2,3,0,1] row_mask:0xf bank_mask:0xf bound_ctrl:1
	buffer_load_dwordx4 v[20:23], v25, s[0:3], s5 offen offset:2048 nt
	buffer_load_dwordx4 v[46:49], v25, s[0:3], s5 offen offset:3072 nt
	v_add_f32_dpp v17, v17, v17 row_ror:4 row_mask:0xf bank_mask:0xf bound_ctrl:1
	v_add_f32_dpp v58, v16, v16 row_ror:8 row_mask:0xf bank_mask:0xf bound_ctrl:1
	buffer_load_dwordx4 v[38:41], v25, s[0:3], s10 offen nt
	buffer_load_dwordx4 v[50:53], v25, s[0:3], s10 offen offset:1024 nt
	v_add_f32_dpp v17, v17, v17 row_ror:8 row_mask:0xf bank_mask:0xf bound_ctrl:1
	v_mov_b32_e32 v19, v17
	v_mov_b32_e32 v59, v58
	s_nop 0
	v_permlane16_swap_b32_e32 v17, v19
	v_permlane16_swap_b32_e32 v58, v59
	v_add_f32_e32 v16, v17, v19
	v_add_f32_e32 v17, v58, v59
	s_add_i32 s5, s4, 0x60000
	s_add_i32 s4, s4, 0x70000
	v_add_f32_dpp v18, v18, v18 quad_perm:[1,0,3,2] row_mask:0xf bank_mask:0xf bound_ctrl:1
	s_waitcnt vmcnt(7)
	v_pk_fma_f32 v[28:29], v[14:15], v[28:29], v[54:55]
	v_pk_fma_f32 v[54:55], v[12:13], v[26:27], v[56:57]
	s_waitcnt vmcnt(6)
	v_pk_fma_f32 v[58:59], v[10:11], v[32:33], v[28:29]
	buffer_load_dwordx4 v[26:29], v25, s[0:3], s10 offen offset:2048 nt
	v_pk_fma_f32 v[54:55], v[8:9], v[30:31], v[54:55]
	buffer_load_dwordx4 v[30:33], v25, s[0:3], s10 offen offset:3072 nt
	v_add_f32_e32 v66, v54, v55
	s_waitcnt vmcnt(7)
	v_pk_mul_f32 v[54:55], v[6:7], v[44:45]
	v_pk_mul_f32 v[56:57], v[4:5], v[42:43]
	buffer_load_dwordx4 v[42:45], v25, s[0:3], s5 offen offset:1024 nt
	s_waitcnt vmcnt(7)
	v_pk_fma_f32 v[54:55], v[2:3], v[36:37], v[54:55]
	v_pk_fma_f32 v[56:57], v[0:1], v[34:35], v[56:57]
	buffer_load_dwordx4 v[34:37], v25, s[0:3], s5 offen nt
	v_add_f32_dpp v18, v18, v18 quad_perm:[2,3,0,1] row_mask:0xf bank_mask:0xf bound_ctrl:1
	s_waitcnt vmcnt(7)
	v_pk_fma_f32 v[22:23], v[14:15], v[22:23], v[54:55]
	v_pk_fma_f32 v[20:21], v[12:13], v[20:21], v[56:57]
	s_waitcnt vmcnt(6)
	v_pk_fma_f32 v[60:61], v[10:11], v[48:49], v[22:23]
	v_pk_fma_f32 v[22:23], v[8:9], v[46:47], v[20:21]
	s_waitcnt vmcnt(4)
	v_pk_mul_f32 v[54:55], v[4:5], v[50:51]
	v_pk_mul_f32 v[20:21], v[6:7], v[52:53]
	v_pk_fma_f32 v[38:39], v[0:1], v[38:39], v[54:55]
	buffer_load_dwordx4 v[46:49], v25, s[0:3], s5 offen offset:2048 nt
	buffer_load_dwordx4 v[50:53], v25, s[0:3], s5 offen offset:3072 nt
	v_pk_fma_f32 v[20:21], v[2:3], v[40:41], v[20:21]
	v_add_f32_e32 v23, v22, v23
	v_add_f32_dpp v18, v18, v18 row_ror:4 row_mask:0xf bank_mask:0xf bound_ctrl:1
	s_waitcnt vmcnt(5)
	v_pk_fma_f32 v[26:27], v[12:13], v[26:27], v[38:39]
	buffer_load_dwordx4 v[38:41], v25, s[0:3], s4 offen nt
	buffer_load_dwordx4 v[54:57], v25, s[0:3], s4 offen offset:1024 nt
	v_pk_fma_f32 v[20:21], v[14:15], v[28:29], v[20:21]
	s_waitcnt vmcnt(6)
	v_pk_fma_f32 v[30:31], v[8:9], v[30:31], v[26:27]
	v_pk_fma_f32 v[62:63], v[10:11], v[32:33], v[20:21]
	v_add_f32_dpp v18, v18, v18 row_ror:8 row_mask:0xf bank_mask:0xf bound_ctrl:1
	s_waitcnt vmcnt(5)
	v_pk_mul_f32 v[20:21], v[6:7], v[44:45]
	v_pk_mul_f32 v[26:27], v[4:5], v[42:43]
	buffer_load_dwordx4 v[42:45], v25, s[0:3], s4 offen offset:2048 nt
	s_waitcnt vmcnt(5)
	v_pk_fma_f32 v[64:65], v[0:1], v[34:35], v[26:27]
	buffer_load_dwordx4 v[32:35], v25, s[0:3], s4 offen offset:3072 nt
	v_add_f32_e32 v27, v60, v61
	v_add_f32_e32 v23, v23, v27
	v_pk_fma_f32 v[36:37], v[2:3], v[36:37], v[20:21]
	v_add_f32_e32 v20, v58, v59
	v_add_f32_dpp v23, v23, v23 quad_perm:[1,0,3,2] row_mask:0xf bank_mask:0xf bound_ctrl:1
	v_add_f32_e32 v20, v66, v20
	v_mov_b32_e32 v19, v18
	v_add_f32_dpp v23, v23, v23 quad_perm:[2,3,0,1] row_mask:0xf bank_mask:0xf bound_ctrl:1
	v_add_f32_dpp v20, v20, v20 quad_perm:[1,0,3,2] row_mask:0xf bank_mask:0xf bound_ctrl:1
	v_permlane16_swap_b32_e32 v18, v19
	v_add_f32_dpp v23, v23, v23 row_ror:4 row_mask:0xf bank_mask:0xf bound_ctrl:1
	v_add_f32_dpp v20, v20, v20 quad_perm:[2,3,0,1] row_mask:0xf bank_mask:0xf bound_ctrl:1
	v_add_f32_e32 v18, v18, v19
	v_add_f32_dpp v23, v23, v23 row_ror:8 row_mask:0xf bank_mask:0xf bound_ctrl:1
	v_mov_b32_e32 v27, v23
	s_nop 1
	v_permlane16_swap_b32_e32 v23, v27
	v_add_f32_e32 v28, v23, v27
	v_add_f32_e32 v23, v30, v31
	s_waitcnt vmcnt(5)
	v_pk_fma_f32 v[30:31], v[14:15], v[48:49], v[36:37]
	v_pk_fma_f32 v[36:37], v[12:13], v[46:47], v[64:65]
	s_waitcnt vmcnt(4)
	v_pk_fma_f32 v[30:31], v[10:11], v[52:53], v[30:31]
	v_pk_fma_f32 v[36:37], v[8:9], v[50:51], v[36:37]
	v_add_f32_e32 v27, v62, v63
	v_add_f32_e32 v36, v36, v37
	v_add_f32_e32 v30, v30, v31
	v_add_f32_e32 v23, v23, v27
	v_add_f32_e32 v30, v36, v30
	v_add_f32_dpp v20, v20, v20 row_ror:4 row_mask:0xf bank_mask:0xf bound_ctrl:1
	v_add_f32_dpp v23, v23, v23 quad_perm:[1,0,3,2] row_mask:0xf bank_mask:0xf bound_ctrl:1
	v_add_f32_dpp v30, v30, v30 quad_perm:[1,0,3,2] row_mask:0xf bank_mask:0xf bound_ctrl:1
	v_add_f32_dpp v20, v20, v20 row_ror:8 row_mask:0xf bank_mask:0xf bound_ctrl:1
	v_add_f32_dpp v23, v23, v23 quad_perm:[2,3,0,1] row_mask:0xf bank_mask:0xf bound_ctrl:1
	v_add_f32_dpp v30, v30, v30 quad_perm:[2,3,0,1] row_mask:0xf bank_mask:0xf bound_ctrl:1
	v_mov_b32_e32 v21, v20
	v_add_f32_dpp v23, v23, v23 row_ror:4 row_mask:0xf bank_mask:0xf bound_ctrl:1
	v_add_f32_dpp v30, v30, v30 row_ror:4 row_mask:0xf bank_mask:0xf bound_ctrl:1
	v_permlane16_swap_b32_e32 v20, v21
	v_add_f32_dpp v23, v23, v23 row_ror:8 row_mask:0xf bank_mask:0xf bound_ctrl:1
	v_add_f32_dpp v30, v30, v30 row_ror:8 row_mask:0xf bank_mask:0xf bound_ctrl:1
	v_mov_b32_e32 v27, v23
	v_mov_b32_e32 v31, v30
	s_nop 0
	v_permlane16_swap_b32_e32 v23, v27
	v_permlane16_swap_b32_e32 v30, v31
	v_add_f32_e32 v21, v20, v21
	v_add_f32_e32 v23, v23, v27
	v_add_f32_e32 v30, v30, v31
	v_mov_b32_e32 v19, v16
	v_mov_b32_e32 v20, v17
	v_mov_b32_e32 v22, v18
	v_mov_b32_e32 v26, v21
	v_mov_b32_e32 v29, v28
	v_mov_b32_e32 v27, v23
	v_mov_b32_e32 v31, v30
	v_permlane32_swap_b32_e32 v16, v19
	v_permlane32_swap_b32_e32 v17, v20
	v_permlane32_swap_b32_e32 v18, v22
	v_permlane32_swap_b32_e32 v21, v26
	v_permlane32_swap_b32_e32 v28, v29
	v_permlane32_swap_b32_e32 v23, v27
	v_permlane32_swap_b32_e32 v30, v31
	v_add_f32_e32 v60, v16, v19
	v_cmp_eq_u32_e32 vcc, 0, v24
	v_add_f32_e32 v61, v17, v20
	v_add_f32_e32 v62, v18, v22
	v_cndmask_b32_e32 v60, 0, v60, vcc
	v_cmp_eq_u32_e32 vcc, 1, v24
	v_add_f32_e32 v63, v21, v26
	v_add_f32_e32 v64, v28, v29
	v_cndmask_b32_e32 v60, v60, v61, vcc
	v_cmp_eq_u32_e32 vcc, 2, v24
	v_add_f32_e32 v65, v23, v27
	v_add_f32_e32 v66, v30, v31
	v_cndmask_b32_e32 v60, v60, v62, vcc
	v_cmp_eq_u32_e32 vcc, 3, v24
	s_lshl_b32 s0, s8, 13
	s_lshr_b32 s1, s9, 4
	v_cndmask_b32_e32 v60, v60, v63, vcc
	v_cmp_eq_u32_e32 vcc, 4, v24
	s_lshl_b32 s1, s1, 2
	s_add_i32 s0, s0, s1
	v_cndmask_b32_e32 v60, v60, v64, vcc
	v_cmp_eq_u32_e32 vcc, 5, v24
	s_addk_i32 s0, 0x6040
	s_nop 0
	v_cndmask_b32_e32 v60, v60, v65, vcc
	v_cmp_eq_u32_e32 vcc, 6, v24
	v_lshl_add_u32 v61, v24, 2, s0
	s_nop 0
	v_cndmask_b32_e32 v60, v60, v66, vcc
	v_cmp_gt_u32_e64 s[2:3], 8, v24
	v_cmp_eq_u32_e32 vcc, 7, v24
	s_waitcnt vmcnt(2)
	v_pk_mul_f32 v[6:7], v[6:7], v[56:57]
	v_pk_mul_f32 v[4:5], v[4:5], v[54:55]
	v_pk_fma_f32 v[2:3], v[2:3], v[40:41], v[6:7]
	v_pk_fma_f32 v[0:1], v[0:1], v[38:39], v[4:5]
	s_waitcnt vmcnt(1)
	v_pk_fma_f32 v[2:3], v[14:15], v[44:45], v[2:3]
	v_pk_fma_f32 v[0:1], v[12:13], v[42:43], v[0:1]
	s_waitcnt vmcnt(0)
	v_pk_fma_f32 v[2:3], v[10:11], v[34:35], v[2:3]
	v_pk_fma_f32 v[0:1], v[8:9], v[32:33], v[0:1]
	s_nop 0
	v_add_f32_e32 v0, v0, v1
	v_add_f32_e32 v1, v2, v3
	v_add_f32_e32 v0, v0, v1
	s_nop 1
	v_add_f32_dpp v0, v0, v0 quad_perm:[1,0,3,2] row_mask:0xf bank_mask:0xf bound_ctrl:1
	s_nop 1
	v_add_f32_dpp v0, v0, v0 quad_perm:[2,3,0,1] row_mask:0xf bank_mask:0xf bound_ctrl:1
	s_nop 1
	v_add_f32_dpp v0, v0, v0 row_ror:4 row_mask:0xf bank_mask:0xf bound_ctrl:1
	s_nop 1
	v_add_f32_dpp v0, v0, v0 row_ror:8 row_mask:0xf bank_mask:0xf bound_ctrl:1
	v_mov_b32_e32 v1, v0
	s_nop 1
	v_permlane16_swap_b32_e32 v0, v1
	v_add_f32_e32 v0, v0, v1
	v_mov_b32_e32 v1, v0
	s_nop 1
	v_permlane32_swap_b32_e32 v0, v1
	v_add_f32_e32 v0, v0, v1
	v_cndmask_b32_e32 v60, v60, v0, vcc
	s_and_saveexec_b64 s[0:1], s[2:3]
	global_store_dword v61, v60, s[6:7]
	s_endpgm
